# layers 1 and 3 sweep their tiles (and so the f16 edge stream) in reverse order, layer 2 forward: most recently used end of the stream is re-read first from the last-level cache
# speedup vs baseline: 1.0280x; 1.0012x over previous
.LBB5_4:
	s_mov_b64 s[4:5], s[28:29]
	s_ashr_i32 s2, s2, 3
	s_add_i32 s25, s11, s2
	s_bitcmp1_b32 s26, 2
	s_cbranch_scc0 .Llay_fwd
	s_sub_i32 s25, 0xc34, s25
.Llay_fwd:
	v_lshrrev_b32_e32 v35, 3, v0
	s_lshl_b32 s24, s25, 5
	v_and_b32_e32 v60, 30, v35
	v_or_b32_e32 v8, s24, v60
	v_min_i32_e32 v2, 0x1869f, v8
	v_ashrrev_i32_e32 v3, 31, v2
	v_and_b32_e32 v1, 15, v0
	v_lshlrev_b64 v[2:3], 8, v[2:3]
	v_mov_b32_e32 v27, 0
	v_lshl_add_u64 v[2:3], s[4:5], 0, v[2:3]
	v_lshlrev_b32_e32 v26, 4, v1
	v_lshl_add_u64 v[2:3], v[2:3], 0, v[26:27]
	global_load_dwordx4 v[2:5], v[2:3], off
	v_cmp_gt_u32_e32 vcc, 33, v0
	s_and_saveexec_b64 s[2:3], vcc
	s_cbranch_execz .LBB5_6
	v_add_u32_e32 v6, s24, v0
	v_min_i32_e32 v6, 0x186a0, v6
	v_ashrrev_i32_e32 v7, 31, v6
	v_lshl_add_u64 v[6:7], v[6:7], 2, s[8:9]
	global_load_dword v6, v[6:7], off
	v_lshlrev_b32_e32 v7, 2, v0
	s_waitcnt vmcnt(0)
	ds_write_b32 v7, v6 offset:12800
